# static s_setprio 1 for waves 4-7 across phases P, B1, B (GLA + attention), reset before F
# baseline (speedup 1.0000x reference)
; #define LAS __attribute__((address_space(3)))
; DI int lbid() { int t = blockIdx.x; asm volatile("" : "+s"(t)); return t; }
; #define CTX const Ctx c = load_ctx(); const int G = lgrid(); LAS unsigned char* lds = LDSBASE
; DI void phase_p(LAS unsigned char* lds, const Ctx& c, int l, int G) {
;     int h_loaded = -1;
;     for (int u = lbid(); u < 8 * 4 * 64; u += G) gla_p_unit(lds, c, l, u >> 8, (u >> 6) & 3, u & 63, h_loaded);
; }
; __global__ void __launch_bounds__(NTHREADS, 2) mk_fwd(Ctx c_arg) {
;     ...
;             if (RUN) { CTX; phase_p(lds, c, l, G); }
.LBB0_560:
	v_readlane_b32 s8, v253, 0
	v_readlane_b32 s10, v253, 2
	s_cmp_ge_i32 s4, s10
	s_cselect_b64 s[4:5], -1, 0
	s_and_b64 s[0:1], s[4:5], s[0:1]
	s_andn2_b64 vcc, exec, s[0:1]
	v_readlane_b32 s9, v253, 1
	v_readlane_b32 s11, v253, 3
	s_cbranch_vccnz .LBB0_582
	v_readfirstlane_b32 s100, v0
	s_lshr_b32 s100, s100, 8
	s_cmp_eq_u32 s100, 0
	s_cbranch_scc1 .Lprio_p
	s_setprio 1
.Lprio_p:
	v_readlane_b32 s4, v253, 7
	s_mov_b64 s[16:17], s[84:85]
	v_readlane_b32 s5, v253, 8
	s_load_dword s4, s[4:5], 0x0
	s_mov_b32 s5, s69
	s_mov_b32 s38, s2
	s_waitcnt lgkmcnt(0)
	s_cmpk_gt_i32 s38, 0x7ff
	s_cbranch_scc1 .LBB0_582
	s_load_dwordx2 s[6:7], s[16:17], 0x98
	s_load_dwordx4 s[40:43], s[16:17], 0x18
	s_add_i32 s39, s5, 0x10c00
	s_add_i32 s48, s5, 0x13000
	s_add_i32 s49, s5, 0x15000
	s_waitcnt lgkmcnt(0)
	s_add_u32 s50, s6, 0x20bc0000
	s_addc_u32 s51, s7, 0
	s_add_u32 s52, s6, 0x22bc0000
	s_addc_u32 s53, s7, 0
	s_add_u32 s54, s6, 0x24bc0000
	s_addc_u32 s55, s7, 0
	s_add_u32 s56, s6, 0x209c0000
	s_addc_u32 s57, s7, 0
	s_add_u32 s58, s6, 0x46bc0000
	s_addc_u32 s59, s7, 0
	v_readlane_b32 s8, v254, 55
	s_add_u32 s16, s40, s8
	s_addc_u32 s17, s41, 0
	s_add_u32 s60, s6, 0x1c9c0000
	s_addc_u32 s61, s7, 0
	s_add_i32 s62, s5, 0x13800
	s_mov_b32 s63, -1
	s_branch .LBB0_564

; #define CTX const Ctx c = load_ctx(); const int G = lgrid(); LAS unsigned char* lds = LDSBASE
; #define END_STEP do { if (RUN && step + 1 < hi) { if (!MK_MULTI) xcd_barrier(bar); } ++step; } while (0)
; DI void xcd_barrier(const XcdBarrier& b) {
;     asm volatile("s_waitcnt vmcnt(0)" ::: "memory");
;     __syncthreads();
;     if (threadIdx.x == 0) {
;         unsigned* bar = b.bar;
;         __builtin_amdgcn_s_waitcnt(0);
;         unsigned nloc = b.st[0], nx = b.st[1];
;         if (nloc == 0u) { xcd_barrier_complete(bar, b.x, nloc, nx); b.st[0] = nloc; b.st[1] = nx; }
; __global__ void __launch_bounds__(NTHREADS, 2) mk_fwd(Ctx c_arg) {
;     ...
;             if (RUN) { CTX; phase_b(lds, c, l, hf, G); }
;             END_STEP;
;             if (RUN) { CTX; (void)lds; phase_f(c, G); }
.LBB0_820:
	s_setprio 0
	v_readlane_b32 s8, v253, 0
	s_add_i32 s4, s13, 4
	v_readlane_b32 s11, v253, 3
	s_cmp_lt_i32 s4, s11
	s_cselect_b64 s[16:17], -1, 0
	s_and_b64 s[0:1], s[0:1], s[16:17]
	s_andn2_b64 vcc, exec, s[0:1]
	v_readlane_b32 s9, v253, 1
	v_readlane_b32 s10, v253, 2
	s_cbranch_vccnz .LBB0_866
	s_waitcnt vmcnt(0)
	s_waitcnt vmcnt(0) lgkmcnt(0)
	s_barrier
	s_mov_b64 s[0:1], exec
	v_readlane_b32 s6, v253, 4
	v_readlane_b32 s7, v253, 5
	s_and_b64 s[6:7], s[0:1], s[6:7]
	s_mov_b64 exec, s[6:7]
	s_cbranch_execz .LBB0_865
	v_readlane_b32 s5, v253, 6
	s_waitcnt vmcnt(0) expcnt(0) lgkmcnt(0)
	s_nop 0
	v_mov_b32_e32 v1, s5
	ds_read_b32 v6, v1
	v_readlane_b32 s5, v253, 9
	s_waitcnt lgkmcnt(0)
	v_cmp_ne_u32_e32 vcc, 0, v6
	v_mov_b32_e32 v1, s5
	ds_read_b32 v2, v1
	s_cbranch_vccnz .LBB0_836
	v_readlane_b32 s8, v253, 7
	v_readlane_b32 s9, v253, 8
	s_load_dwordx2 s[6:7], s[8:9], 0x0
	s_nop 0
	s_load_dword s8, s[8:9], 0x8
	s_mov_b32 s5, 1
	s_mov_b64 s[30:31], 0
	s_waitcnt lgkmcnt(0)
	s_mul_i32 s6, s7, s6
	s_mul_i32 s6, s6, s8
	s_branch .LBB0_826

; __global__ void __launch_bounds__(NTHREADS, 2) mk_fwd(Ctx c_arg) {
	.amdhsa_kernel _Z6mk_fwd3Ctx
		.amdhsa_group_segment_fixed_size 0
		.amdhsa_private_segment_fixed_size 0
		.amdhsa_kernarg_size 424
		.amdhsa_user_sgpr_count 2
		.amdhsa_user_sgpr_dispatch_ptr 0
		.amdhsa_user_sgpr_queue_ptr 0
		.amdhsa_user_sgpr_kernarg_segment_ptr 1
		.amdhsa_user_sgpr_dispatch_id 0
		.amdhsa_user_sgpr_kernarg_preload_length 0
		.amdhsa_user_sgpr_kernarg_preload_offset 0
		.amdhsa_user_sgpr_private_segment_size 0
		.amdhsa_uses_dynamic_stack 0
		.amdhsa_enable_private_segment 0
		.amdhsa_system_sgpr_workgroup_id_x 1
		.amdhsa_system_sgpr_workgroup_id_y 0
		.amdhsa_system_sgpr_workgroup_id_z 0
		.amdhsa_system_sgpr_workgroup_info 0
		.amdhsa_system_vgpr_workitem_id 0
		.amdhsa_next_free_vgpr 256
		.amdhsa_next_free_sgpr 102
		.amdhsa_accum_offset 256
		.amdhsa_reserve_vcc 1
		.amdhsa_float_round_mode_32 0
		.amdhsa_float_round_mode_16_64 0
		.amdhsa_float_denorm_mode_32 3
		.amdhsa_float_denorm_mode_16_64 3
		.amdhsa_dx10_clamp 1
		.amdhsa_ieee_mode 1
		.amdhsa_fp16_overflow 0
		.amdhsa_tg_split 0
		.amdhsa_exception_fp_ieee_invalid_op 0
		.amdhsa_exception_fp_denorm_src 0
		.amdhsa_exception_fp_ieee_div_zero 0
		.amdhsa_exception_fp_ieee_overflow 0
		.amdhsa_exception_fp_ieee_underflow 0
		.amdhsa_exception_fp_ieee_inexact 0
		.amdhsa_exception_int_div_zero 0
	.end_amdhsa_kernel

; __global__ void __launch_bounds__(NTHREADS, 2) mk_fwd(Ctx c_arg) {
amdhsa.kernels:
  - .agpr_count:     0
    .args:
      - .offset:         0
        .size:           168
        .value_kind:     by_value
      - .offset:         168
        .size:           4
        .value_kind:     hidden_block_count_x
      - .offset:         172
        .size:           4
        .value_kind:     hidden_block_count_y
      - .offset:         176
        .size:           4
        .value_kind:     hidden_block_count_z
      - .offset:         180
        .size:           2
        .value_kind:     hidden_group_size_x
      - .offset:         182
        .size:           2
        .value_kind:     hidden_group_size_y
      - .offset:         184
        .size:           2
        .value_kind:     hidden_group_size_z
      - .offset:         186
        .size:           2
        .value_kind:     hidden_remainder_x
      - .offset:         188
        .size:           2
        .value_kind:     hidden_remainder_y
      - .offset:         190
        .size:           2
        .value_kind:     hidden_remainder_z
      - .offset:         208
        .size:           8
        .value_kind:     hidden_global_offset_x
      - .offset:         216
        .size:           8
        .value_kind:     hidden_global_offset_y
      - .offset:         224
        .size:           8
        .value_kind:     hidden_global_offset_z
      - .offset:         232
        .size:           2
        .value_kind:     hidden_grid_dims
      - .offset:         288
        .size:           4
        .value_kind:     hidden_dynamic_lds_size
    .group_segment_fixed_size: 0
    .kernarg_segment_align: 8
    .kernarg_segment_size: 424
    .language:       OpenCL C
    .language_version:
      - 2
      - 0
    .max_flat_workgroup_size: 512
    .name:           _Z6mk_fwd3Ctx
    .private_segment_fixed_size: 0
    .sgpr_count:     108
    .sgpr_spill_count: 301
    .symbol:         _Z6mk_fwd3Ctx.kd
    .uniform_work_group_size: 1
    .uses_dynamic_stack: false
    .vgpr_count:     256
    .vgpr_spill_count: 0
    .wavefront_size: 64
